# P6 SwiGLU epilogue: two store chunks (16 elements) interleaved per math group for more ILP; zero-inits dropped
# speedup vs baseline: 1.0017x; 1.0017x over previous
; __device__ __forceinline__ unsigned pk4_fp8(float a, float b, float c, float d) { int r = __builtin_amdgcn_cvt_pk_fp8_f32(a, b, 0, false); r = __builtin_amdgcn_cvt_pk_fp8_f32(c, d, r, true); return (unsigned)r; }
;     __device__ __forceinline__ void operator()(const f32x4 (&acc)[2][2][4][2], const Unit& u, int wr, int wc, int fr, int fq) const {
;         const int row0 = u.pm * BM + wr * 64 + fr, col0 = (u.pn & 3) * 128 + wc * 32 + 8 * fq;
; #pragma unroll
;         for (int ai = 0; ai < 2; ++ai)
; #pragma unroll
;             for (int m = 0; m < 4; ++m) { float r[8];
; #pragma unroll
;                 for (int n = 0; n < 2; ++n)
; #pragma unroll
;                     for (int e = 0; e < 4; ++e) { const float g = acc[ai][0][m][n][e], up = acc[ai][1][m][n][e]; r[4 * n + e] = g * __builtin_amdgcn_rcpf(1.0f + __builtin_amdgcn_exp2f(-g * LOG2E)) * up * (float)(1 << ASHIFT); }
;                 v2u w; w.x = pk4_fp8(r[0], r[1], r[2], r[3]); w.y = pk4_fp8(r[4], r[5], r[6], r[7]);
;                 *(v2u*)(O + (size_t)(row0 + ai * HALF + m * 16) * EH + col0) = w; }
;     }
.LBB0_751:
	s_mov_b32 s98, 0xbfb8aa3b
	s_mov_b32 s100, 0x41800000
	s_nop 15
	s_nop 15
	v_lshl_add_u32 v4, s88, 8, v203
	s_lshl_b32 s6, s89, 7
	s_and_b32 s6, s6, 0x180
	v_ashrrev_i32_e32 v5, 31, v4
	v_add_u32_e32 v2, s6, v205
	v_lshlrev_b64 v[0:1], 9, v[4:5]
	v_ashrrev_i32_e32 v3, 31, v2
	v_lshl_add_u64 v[0:1], s[24:25], 0, v[0:1]
	v_lshl_add_u64 v[0:1], v[0:1], 0, v[2:3]
	v_pk_mul_f32 v[228:229], v[192:193], s[98:99] op_sel_hi:[1,0]
	v_pk_mul_f32 v[230:231], v[194:195], s[98:99] op_sel_hi:[1,0]
	v_pk_mul_f32 v[232:233], v[184:185], s[98:99] op_sel_hi:[1,0]
	v_pk_mul_f32 v[234:235], v[186:187], s[98:99] op_sel_hi:[1,0]
	v_pk_mul_f32 v[236:237], v[176:177], s[98:99] op_sel_hi:[1,0]
	v_pk_mul_f32 v[238:239], v[178:179], s[98:99] op_sel_hi:[1,0]
	v_pk_mul_f32 v[240:241], v[168:169], s[98:99] op_sel_hi:[1,0]
	v_pk_mul_f32 v[242:243], v[170:171], s[98:99] op_sel_hi:[1,0]
	v_exp_f32_e32 v228, v228
	v_exp_f32_e32 v229, v229
	v_exp_f32_e32 v230, v230
	v_exp_f32_e32 v231, v231
	v_exp_f32_e32 v232, v232
	v_exp_f32_e32 v233, v233
	v_exp_f32_e32 v234, v234
	v_exp_f32_e32 v235, v235
	v_exp_f32_e32 v236, v236
	v_exp_f32_e32 v237, v237
	v_exp_f32_e32 v238, v238
	v_exp_f32_e32 v239, v239
	v_exp_f32_e32 v240, v240
	v_exp_f32_e32 v241, v241
	v_exp_f32_e32 v242, v242
	v_exp_f32_e32 v243, v243
	v_pk_add_f32 v[228:229], v[228:229], 1.0 op_sel_hi:[1,0]
	v_pk_add_f32 v[230:231], v[230:231], 1.0 op_sel_hi:[1,0]
	v_pk_add_f32 v[232:233], v[232:233], 1.0 op_sel_hi:[1,0]
	v_pk_add_f32 v[234:235], v[234:235], 1.0 op_sel_hi:[1,0]
	v_pk_add_f32 v[236:237], v[236:237], 1.0 op_sel_hi:[1,0]
	v_pk_add_f32 v[238:239], v[238:239], 1.0 op_sel_hi:[1,0]
	v_pk_add_f32 v[240:241], v[240:241], 1.0 op_sel_hi:[1,0]
	v_pk_add_f32 v[242:243], v[242:243], 1.0 op_sel_hi:[1,0]
	v_rcp_f32_e32 v228, v228
	v_rcp_f32_e32 v229, v229
	v_rcp_f32_e32 v230, v230
	v_rcp_f32_e32 v231, v231
	v_rcp_f32_e32 v232, v232
	v_rcp_f32_e32 v233, v233
	v_rcp_f32_e32 v234, v234
	v_rcp_f32_e32 v235, v235
	v_rcp_f32_e32 v236, v236
	v_rcp_f32_e32 v237, v237
	v_rcp_f32_e32 v238, v238
	v_rcp_f32_e32 v239, v239
	v_rcp_f32_e32 v240, v240
	v_rcp_f32_e32 v241, v241
	v_rcp_f32_e32 v242, v242
	v_rcp_f32_e32 v243, v243
	v_pk_mul_f32 v[228:229], v[192:193], v[228:229]
	v_pk_mul_f32 v[230:231], v[194:195], v[230:231]
	v_pk_mul_f32 v[232:233], v[184:185], v[232:233]
	v_pk_mul_f32 v[234:235], v[186:187], v[234:235]
	v_pk_mul_f32 v[236:237], v[176:177], v[236:237]
	v_pk_mul_f32 v[238:239], v[178:179], v[238:239]
	v_pk_mul_f32 v[240:241], v[168:169], v[240:241]
	v_pk_mul_f32 v[242:243], v[170:171], v[242:243]
	v_pk_mul_f32 v[228:229], v[188:189], v[228:229]
	v_pk_mul_f32 v[230:231], v[190:191], v[230:231]
	v_pk_mul_f32 v[232:233], v[180:181], v[232:233]
	v_pk_mul_f32 v[234:235], v[182:183], v[234:235]
	v_pk_mul_f32 v[236:237], v[172:173], v[236:237]
	v_pk_mul_f32 v[238:239], v[174:175], v[238:239]
	v_pk_mul_f32 v[240:241], v[164:165], v[240:241]
	v_pk_mul_f32 v[242:243], v[166:167], v[242:243]
	v_pk_mul_f32 v[228:229], s[100:101], v[228:229] op_sel_hi:[0,1]
	v_pk_mul_f32 v[230:231], s[100:101], v[230:231] op_sel_hi:[0,1]
	v_pk_mul_f32 v[232:233], s[100:101], v[232:233] op_sel_hi:[0,1]
	v_pk_mul_f32 v[234:235], s[100:101], v[234:235] op_sel_hi:[0,1]
	v_pk_mul_f32 v[236:237], s[100:101], v[236:237] op_sel_hi:[0,1]
	v_pk_mul_f32 v[238:239], s[100:101], v[238:239] op_sel_hi:[0,1]
	v_pk_mul_f32 v[240:241], s[100:101], v[240:241] op_sel_hi:[0,1]
	v_pk_mul_f32 v[242:243], s[100:101], v[242:243] op_sel_hi:[0,1]
	v_cvt_pk_fp8_f32 v244, v228, v229
	v_cvt_pk_fp8_f32 v245, v232, v233
	v_cvt_pk_fp8_f32 v246, v236, v237
	v_cvt_pk_fp8_f32 v247, v240, v241
	v_cvt_pk_fp8_f32 v244, v230, v231 op_sel:[0,0,1]
	v_cvt_pk_fp8_f32 v245, v234, v235 op_sel:[0,0,1]
	v_cvt_pk_fp8_f32 v246, v238, v239 op_sel:[0,0,1]
	v_cvt_pk_fp8_f32 v247, v242, v243 op_sel:[0,0,1]
	s_nop 0
	global_store_dwordx2 v[0:1], v[244:245], off
	v_or_b32_e32 v8, 16, v4
	v_ashrrev_i32_e32 v9, 31, v8
	v_lshlrev_b64 v[8:9], 9, v[8:9]
	v_lshl_add_u64 v[8:9], s[24:25], 0, v[8:9]
	v_lshl_add_u64 v[8:9], v[8:9], 0, v[2:3]
	global_store_dwordx2 v[8:9], v[246:247], off
	v_or_b32_e32 v8, 32, v4
	v_ashrrev_i32_e32 v9, 31, v8
	v_lshlrev_b64 v[8:9], 9, v[8:9]
	v_lshl_add_u64 v[8:9], s[24:25], 0, v[8:9]
	v_lshl_add_u64 v[8:9], v[8:9], 0, v[2:3]
	v_pk_mul_f32 v[228:229], v[160:161], s[98:99] op_sel_hi:[1,0]
	v_pk_mul_f32 v[230:231], v[162:163], s[98:99] op_sel_hi:[1,0]
	v_pk_mul_f32 v[232:233], v[152:153], s[98:99] op_sel_hi:[1,0]
	v_pk_mul_f32 v[234:235], v[154:155], s[98:99] op_sel_hi:[1,0]
	v_pk_mul_f32 v[236:237], v[144:145], s[98:99] op_sel_hi:[1,0]
	v_pk_mul_f32 v[238:239], v[146:147], s[98:99] op_sel_hi:[1,0]
	v_pk_mul_f32 v[240:241], v[136:137], s[98:99] op_sel_hi:[1,0]
	v_pk_mul_f32 v[242:243], v[138:139], s[98:99] op_sel_hi:[1,0]
	v_exp_f32_e32 v228, v228
	v_exp_f32_e32 v229, v229
	v_exp_f32_e32 v230, v230
	v_exp_f32_e32 v231, v231
	v_exp_f32_e32 v232, v232
	v_exp_f32_e32 v233, v233
	v_exp_f32_e32 v234, v234
	v_exp_f32_e32 v235, v235
	v_exp_f32_e32 v236, v236
	v_exp_f32_e32 v237, v237
	v_exp_f32_e32 v238, v238
	v_exp_f32_e32 v239, v239
	v_exp_f32_e32 v240, v240
	v_exp_f32_e32 v241, v241
	v_exp_f32_e32 v242, v242
	v_exp_f32_e32 v243, v243
	v_pk_add_f32 v[228:229], v[228:229], 1.0 op_sel_hi:[1,0]
	v_pk_add_f32 v[230:231], v[230:231], 1.0 op_sel_hi:[1,0]
	v_pk_add_f32 v[232:233], v[232:233], 1.0 op_sel_hi:[1,0]
	v_pk_add_f32 v[234:235], v[234:235], 1.0 op_sel_hi:[1,0]
	v_pk_add_f32 v[236:237], v[236:237], 1.0 op_sel_hi:[1,0]
	v_pk_add_f32 v[238:239], v[238:239], 1.0 op_sel_hi:[1,0]
	v_pk_add_f32 v[240:241], v[240:241], 1.0 op_sel_hi:[1,0]
	v_pk_add_f32 v[242:243], v[242:243], 1.0 op_sel_hi:[1,0]
; __device__ __forceinline__ unsigned pk4_fp8(float a, float b, float c, float d) { int r = __builtin_amdgcn_cvt_pk_fp8_f32(a, b, 0, false); r = __builtin_amdgcn_cvt_pk_fp8_f32(c, d, r, true); return (unsigned)r; }
;     __device__ __forceinline__ void operator()(const f32x4 (&acc)[2][2][4][2], const Unit& u, int wr, int wc, int fr, int fq) const {
;         const int row0 = u.pm * BM + wr * 64 + fr, col0 = (u.pn & 3) * 128 + wc * 32 + 8 * fq;
; #pragma unroll
;         for (int ai = 0; ai < 2; ++ai)
; #pragma unroll
;             for (int m = 0; m < 4; ++m) { float r[8];
; #pragma unroll
;                 for (int n = 0; n < 2; ++n)
; #pragma unroll
;                     for (int e = 0; e < 4; ++e) { const float g = acc[ai][0][m][n][e], up = acc[ai][1][m][n][e]; r[4 * n + e] = g * __builtin_amdgcn_rcpf(1.0f + __builtin_amdgcn_exp2f(-g * LOG2E)) * up * (float)(1 << ASHIFT); }
;                 v2u w; w.x = pk4_fp8(r[0], r[1], r[2], r[3]); w.y = pk4_fp8(r[4], r[5], r[6], r[7]);
;                 *(v2u*)(O + (size_t)(row0 + ai * HALF + m * 16) * EH + col0) = w; }
;     }
	v_rcp_f32_e32 v228, v228
	v_rcp_f32_e32 v229, v229
	v_rcp_f32_e32 v230, v230
	v_rcp_f32_e32 v231, v231
	v_rcp_f32_e32 v232, v232
	v_rcp_f32_e32 v233, v233
	v_rcp_f32_e32 v234, v234
	v_rcp_f32_e32 v235, v235
	v_rcp_f32_e32 v236, v236
	v_rcp_f32_e32 v237, v237
	v_rcp_f32_e32 v238, v238
	v_rcp_f32_e32 v239, v239
	v_rcp_f32_e32 v240, v240
	v_rcp_f32_e32 v241, v241
	v_rcp_f32_e32 v242, v242
	v_rcp_f32_e32 v243, v243
	v_pk_mul_f32 v[228:229], v[160:161], v[228:229]
	v_pk_mul_f32 v[230:231], v[162:163], v[230:231]
	v_pk_mul_f32 v[232:233], v[152:153], v[232:233]
	v_pk_mul_f32 v[234:235], v[154:155], v[234:235]
	v_pk_mul_f32 v[236:237], v[144:145], v[236:237]
	v_pk_mul_f32 v[238:239], v[146:147], v[238:239]
	v_pk_mul_f32 v[240:241], v[136:137], v[240:241]
	v_pk_mul_f32 v[242:243], v[138:139], v[242:243]
	v_pk_mul_f32 v[228:229], v[156:157], v[228:229]
	v_pk_mul_f32 v[230:231], v[158:159], v[230:231]
	v_pk_mul_f32 v[232:233], v[148:149], v[232:233]
	v_pk_mul_f32 v[234:235], v[150:151], v[234:235]
	v_pk_mul_f32 v[236:237], v[140:141], v[236:237]
	v_pk_mul_f32 v[238:239], v[142:143], v[238:239]
	v_pk_mul_f32 v[240:241], v[132:133], v[240:241]
	v_pk_mul_f32 v[242:243], v[134:135], v[242:243]
	v_pk_mul_f32 v[228:229], s[100:101], v[228:229] op_sel_hi:[0,1]
	v_pk_mul_f32 v[230:231], s[100:101], v[230:231] op_sel_hi:[0,1]
	v_pk_mul_f32 v[232:233], s[100:101], v[232:233] op_sel_hi:[0,1]
	v_pk_mul_f32 v[234:235], s[100:101], v[234:235] op_sel_hi:[0,1]
	v_pk_mul_f32 v[236:237], s[100:101], v[236:237] op_sel_hi:[0,1]
	v_pk_mul_f32 v[238:239], s[100:101], v[238:239] op_sel_hi:[0,1]
	v_pk_mul_f32 v[240:241], s[100:101], v[240:241] op_sel_hi:[0,1]
	v_pk_mul_f32 v[242:243], s[100:101], v[242:243] op_sel_hi:[0,1]
	v_cvt_pk_fp8_f32 v244, v228, v229
	v_cvt_pk_fp8_f32 v245, v232, v233
	v_cvt_pk_fp8_f32 v246, v236, v237
	v_cvt_pk_fp8_f32 v247, v240, v241
	v_cvt_pk_fp8_f32 v244, v230, v231 op_sel:[0,0,1]
	v_cvt_pk_fp8_f32 v245, v234, v235 op_sel:[0,0,1]
	v_cvt_pk_fp8_f32 v246, v238, v239 op_sel:[0,0,1]
	v_cvt_pk_fp8_f32 v247, v242, v243 op_sel:[0,0,1]
	s_nop 0
	global_store_dwordx2 v[8:9], v[244:245], off
	v_or_b32_e32 v4, 48, v4
	v_ashrrev_i32_e32 v5, 31, v4
	v_lshlrev_b64 v[4:5], 9, v[4:5]
	v_lshl_add_u64 v[4:5], s[24:25], 0, v[4:5]
	v_lshl_add_u64 v[2:3], v[4:5], 0, v[2:3]
	global_store_dwordx2 v[2:3], v[246:247], off
	v_add_co_u32_e32 v4, vcc, s50, v0
	s_nop 0
	v_addc_co_u32_e32 v5, vcc, 0, v1, vcc
	v_pk_mul_f32 v[228:229], v[128:129], s[98:99] op_sel_hi:[1,0]
	v_pk_mul_f32 v[230:231], v[130:131], s[98:99] op_sel_hi:[1,0]
	v_pk_mul_f32 v[232:233], v[120:121], s[98:99] op_sel_hi:[1,0]
	v_pk_mul_f32 v[234:235], v[122:123], s[98:99] op_sel_hi:[1,0]
	v_pk_mul_f32 v[236:237], v[112:113], s[98:99] op_sel_hi:[1,0]
	v_pk_mul_f32 v[238:239], v[114:115], s[98:99] op_sel_hi:[1,0]
	v_pk_mul_f32 v[240:241], v[104:105], s[98:99] op_sel_hi:[1,0]
	v_pk_mul_f32 v[242:243], v[106:107], s[98:99] op_sel_hi:[1,0]
	v_exp_f32_e32 v228, v228
	v_exp_f32_e32 v229, v229
	v_exp_f32_e32 v230, v230
	v_exp_f32_e32 v231, v231
	v_exp_f32_e32 v232, v232
	v_exp_f32_e32 v233, v233
	v_exp_f32_e32 v234, v234
	v_exp_f32_e32 v235, v235
	v_exp_f32_e32 v236, v236
	v_exp_f32_e32 v237, v237
	v_exp_f32_e32 v238, v238
	v_exp_f32_e32 v239, v239
	v_exp_f32_e32 v240, v240
	v_exp_f32_e32 v241, v241
	v_exp_f32_e32 v242, v242
	v_exp_f32_e32 v243, v243
	v_pk_add_f32 v[228:229], v[228:229], 1.0 op_sel_hi:[1,0]
	v_pk_add_f32 v[230:231], v[230:231], 1.0 op_sel_hi:[1,0]
	v_pk_add_f32 v[232:233], v[232:233], 1.0 op_sel_hi:[1,0]
	v_pk_add_f32 v[234:235], v[234:235], 1.0 op_sel_hi:[1,0]
	v_pk_add_f32 v[236:237], v[236:237], 1.0 op_sel_hi:[1,0]
	v_pk_add_f32 v[238:239], v[238:239], 1.0 op_sel_hi:[1,0]
	v_pk_add_f32 v[240:241], v[240:241], 1.0 op_sel_hi:[1,0]
	v_pk_add_f32 v[242:243], v[242:243], 1.0 op_sel_hi:[1,0]
	v_rcp_f32_e32 v228, v228
	v_rcp_f32_e32 v229, v229
	v_rcp_f32_e32 v230, v230
	v_rcp_f32_e32 v231, v231
	v_rcp_f32_e32 v232, v232
	v_rcp_f32_e32 v233, v233
	v_rcp_f32_e32 v234, v234
	v_rcp_f32_e32 v235, v235
	v_rcp_f32_e32 v236, v236
	v_rcp_f32_e32 v237, v237
	v_rcp_f32_e32 v238, v238
	v_rcp_f32_e32 v239, v239
	v_rcp_f32_e32 v240, v240
	v_rcp_f32_e32 v241, v241
	v_rcp_f32_e32 v242, v242
	v_rcp_f32_e32 v243, v243
	v_pk_mul_f32 v[228:229], v[128:129], v[228:229]
	v_pk_mul_f32 v[230:231], v[130:131], v[230:231]
	v_pk_mul_f32 v[232:233], v[120:121], v[232:233]
	v_pk_mul_f32 v[234:235], v[122:123], v[234:235]
	v_pk_mul_f32 v[236:237], v[112:113], v[236:237]
	v_pk_mul_f32 v[238:239], v[114:115], v[238:239]
	v_pk_mul_f32 v[240:241], v[104:105], v[240:241]
	v_pk_mul_f32 v[242:243], v[106:107], v[242:243]
	v_pk_mul_f32 v[228:229], v[124:125], v[228:229]
	v_pk_mul_f32 v[230:231], v[126:127], v[230:231]
	v_pk_mul_f32 v[232:233], v[116:117], v[232:233]
	v_pk_mul_f32 v[234:235], v[118:119], v[234:235]
	v_pk_mul_f32 v[236:237], v[108:109], v[236:237]
	v_pk_mul_f32 v[238:239], v[110:111], v[238:239]
	v_pk_mul_f32 v[240:241], v[100:101], v[240:241]
; __device__ __forceinline__ unsigned pk4_fp8(float a, float b, float c, float d) { int r = __builtin_amdgcn_cvt_pk_fp8_f32(a, b, 0, false); r = __builtin_amdgcn_cvt_pk_fp8_f32(c, d, r, true); return (unsigned)r; }
;     __device__ __forceinline__ void operator()(const f32x4 (&acc)[2][2][4][2], const Unit& u, int wr, int wc, int fr, int fq) const {
;         const int row0 = u.pm * BM + wr * 64 + fr, col0 = (u.pn & 3) * 128 + wc * 32 + 8 * fq;
; #pragma unroll
;         for (int ai = 0; ai < 2; ++ai)
; #pragma unroll
;             for (int m = 0; m < 4; ++m) { float r[8];
; #pragma unroll
;                 for (int n = 0; n < 2; ++n)
; #pragma unroll
;                     for (int e = 0; e < 4; ++e) { const float g = acc[ai][0][m][n][e], up = acc[ai][1][m][n][e]; r[4 * n + e] = g * __builtin_amdgcn_rcpf(1.0f + __builtin_amdgcn_exp2f(-g * LOG2E)) * up * (float)(1 << ASHIFT); }
;                 v2u w; w.x = pk4_fp8(r[0], r[1], r[2], r[3]); w.y = pk4_fp8(r[4], r[5], r[6], r[7]);
;                 *(v2u*)(O + (size_t)(row0 + ai * HALF + m * 16) * EH + col0) = w; }
;     }
	v_pk_mul_f32 v[242:243], v[102:103], v[242:243]
	v_pk_mul_f32 v[228:229], s[100:101], v[228:229] op_sel_hi:[0,1]
	v_pk_mul_f32 v[230:231], s[100:101], v[230:231] op_sel_hi:[0,1]
	v_pk_mul_f32 v[232:233], s[100:101], v[232:233] op_sel_hi:[0,1]
	v_pk_mul_f32 v[234:235], s[100:101], v[234:235] op_sel_hi:[0,1]
	v_pk_mul_f32 v[236:237], s[100:101], v[236:237] op_sel_hi:[0,1]
	v_pk_mul_f32 v[238:239], s[100:101], v[238:239] op_sel_hi:[0,1]
	v_pk_mul_f32 v[240:241], s[100:101], v[240:241] op_sel_hi:[0,1]
	v_pk_mul_f32 v[242:243], s[100:101], v[242:243] op_sel_hi:[0,1]
	v_cvt_pk_fp8_f32 v244, v228, v229
	v_cvt_pk_fp8_f32 v245, v232, v233
	v_cvt_pk_fp8_f32 v246, v236, v237
	v_cvt_pk_fp8_f32 v247, v240, v241
	v_cvt_pk_fp8_f32 v244, v230, v231 op_sel:[0,0,1]
	v_cvt_pk_fp8_f32 v245, v234, v235 op_sel:[0,0,1]
	v_cvt_pk_fp8_f32 v246, v238, v239 op_sel:[0,0,1]
	v_cvt_pk_fp8_f32 v247, v242, v243 op_sel:[0,0,1]
	s_nop 0
	global_store_dwordx2 v[4:5], v[244:245], off
	v_add_co_u32_e32 v4, vcc, s52, v0
	s_nop 0
	v_addc_co_u32_e32 v5, vcc, 0, v1, vcc
	global_store_dwordx2 v[4:5], v[246:247], off
	v_add_co_u32_e32 v4, vcc, s54, v0
	s_nop 0
	v_addc_co_u32_e32 v5, vcc, 0, v1, vcc
	v_pk_mul_f32 v[228:229], v[96:97], s[98:99] op_sel_hi:[1,0]
	v_pk_mul_f32 v[230:231], v[98:99], s[98:99] op_sel_hi:[1,0]
	v_pk_mul_f32 v[232:233], v[88:89], s[98:99] op_sel_hi:[1,0]
	v_pk_mul_f32 v[234:235], v[90:91], s[98:99] op_sel_hi:[1,0]
	v_pk_mul_f32 v[236:237], v[80:81], s[98:99] op_sel_hi:[1,0]
	v_pk_mul_f32 v[238:239], v[82:83], s[98:99] op_sel_hi:[1,0]
	v_pk_mul_f32 v[240:241], v[72:73], s[98:99] op_sel_hi:[1,0]
	v_pk_mul_f32 v[242:243], v[74:75], s[98:99] op_sel_hi:[1,0]
	v_exp_f32_e32 v228, v228
	v_exp_f32_e32 v229, v229
	v_exp_f32_e32 v230, v230
	v_exp_f32_e32 v231, v231
	v_exp_f32_e32 v232, v232
	v_exp_f32_e32 v233, v233
	v_exp_f32_e32 v234, v234
	v_exp_f32_e32 v235, v235
	v_exp_f32_e32 v236, v236
	v_exp_f32_e32 v237, v237
	v_exp_f32_e32 v238, v238
	v_exp_f32_e32 v239, v239
	v_exp_f32_e32 v240, v240
	v_exp_f32_e32 v241, v241
	v_exp_f32_e32 v242, v242
	v_exp_f32_e32 v243, v243
	v_pk_add_f32 v[228:229], v[228:229], 1.0 op_sel_hi:[1,0]
	v_pk_add_f32 v[230:231], v[230:231], 1.0 op_sel_hi:[1,0]
	v_pk_add_f32 v[232:233], v[232:233], 1.0 op_sel_hi:[1,0]
	v_pk_add_f32 v[234:235], v[234:235], 1.0 op_sel_hi:[1,0]
	v_pk_add_f32 v[236:237], v[236:237], 1.0 op_sel_hi:[1,0]
	v_pk_add_f32 v[238:239], v[238:239], 1.0 op_sel_hi:[1,0]
	v_pk_add_f32 v[240:241], v[240:241], 1.0 op_sel_hi:[1,0]
	v_pk_add_f32 v[242:243], v[242:243], 1.0 op_sel_hi:[1,0]
	v_rcp_f32_e32 v228, v228
	v_rcp_f32_e32 v229, v229
	v_rcp_f32_e32 v230, v230
	v_rcp_f32_e32 v231, v231
	v_rcp_f32_e32 v232, v232
	v_rcp_f32_e32 v233, v233
	v_rcp_f32_e32 v234, v234
	v_rcp_f32_e32 v235, v235
	v_rcp_f32_e32 v236, v236
	v_rcp_f32_e32 v237, v237
	v_rcp_f32_e32 v238, v238
	v_rcp_f32_e32 v239, v239
	v_rcp_f32_e32 v240, v240
	v_rcp_f32_e32 v241, v241
	v_rcp_f32_e32 v242, v242
	v_rcp_f32_e32 v243, v243
	v_pk_mul_f32 v[228:229], v[96:97], v[228:229]
	v_pk_mul_f32 v[230:231], v[98:99], v[230:231]
	v_pk_mul_f32 v[232:233], v[88:89], v[232:233]
	v_pk_mul_f32 v[234:235], v[90:91], v[234:235]
	v_pk_mul_f32 v[236:237], v[80:81], v[236:237]
	v_pk_mul_f32 v[238:239], v[82:83], v[238:239]
	v_pk_mul_f32 v[240:241], v[72:73], v[240:241]
	v_pk_mul_f32 v[242:243], v[74:75], v[242:243]
	v_pk_mul_f32 v[228:229], v[92:93], v[228:229]
	v_pk_mul_f32 v[230:231], v[94:95], v[230:231]
	v_pk_mul_f32 v[232:233], v[84:85], v[232:233]
	v_pk_mul_f32 v[234:235], v[86:87], v[234:235]
	v_pk_mul_f32 v[236:237], v[76:77], v[236:237]
	v_pk_mul_f32 v[238:239], v[78:79], v[238:239]
	v_pk_mul_f32 v[240:241], v[68:69], v[240:241]
	v_pk_mul_f32 v[242:243], v[70:71], v[242:243]
	v_pk_mul_f32 v[228:229], s[100:101], v[228:229] op_sel_hi:[0,1]
	v_pk_mul_f32 v[230:231], s[100:101], v[230:231] op_sel_hi:[0,1]
	v_pk_mul_f32 v[232:233], s[100:101], v[232:233] op_sel_hi:[0,1]
	v_pk_mul_f32 v[234:235], s[100:101], v[234:235] op_sel_hi:[0,1]
	v_pk_mul_f32 v[236:237], s[100:101], v[236:237] op_sel_hi:[0,1]
	v_pk_mul_f32 v[238:239], s[100:101], v[238:239] op_sel_hi:[0,1]
	v_pk_mul_f32 v[240:241], s[100:101], v[240:241] op_sel_hi:[0,1]
	v_pk_mul_f32 v[242:243], s[100:101], v[242:243] op_sel_hi:[0,1]
	v_cvt_pk_fp8_f32 v244, v228, v229
	v_cvt_pk_fp8_f32 v245, v232, v233
	v_cvt_pk_fp8_f32 v246, v236, v237
	v_cvt_pk_fp8_f32 v247, v240, v241
	v_cvt_pk_fp8_f32 v244, v230, v231 op_sel:[0,0,1]
	v_cvt_pk_fp8_f32 v245, v234, v235 op_sel:[0,0,1]
	v_cvt_pk_fp8_f32 v246, v238, v239 op_sel:[0,0,1]
	v_cvt_pk_fp8_f32 v247, v242, v243 op_sel:[0,0,1]
	s_nop 0
	global_store_dwordx2 v[4:5], v[244:245], off
	v_add_co_u32_e32 v0, vcc, 0x16000, v0
	s_nop 1
	v_addc_co_u32_e32 v1, vcc, 0, v1, vcc
	s_and_b64 vcc, exec, s[4:5]
	s_mov_b64 s[4:5], -1
	global_store_dwordx2 v[0:1], v[246:247], off
	s_cbranch_vccnz .LBB0_715
	s_andn2_b64 vcc, exec, s[22:23]
	s_cbranch_vccnz .LBB0_714
	s_barrier
	s_branch .LBB0_714

; __device__ __forceinline__ unsigned pk4_fp8(float a, float b, float c, float d) { int r = __builtin_amdgcn_cvt_pk_fp8_f32(a, b, 0, false); r = __builtin_amdgcn_cvt_pk_fp8_f32(c, d, r, true); return (unsigned)r; }
;     __device__ __forceinline__ void operator()(const f32x4 (&acc)[2][2][4][2], const Unit& u, int wr, int wc, int fr, int fq) const {
;         const int row0 = u.pm * BM + wr * 64 + fr, col0 = (u.pn & 3) * 128 + wc * 32 + 8 * fq;
; #pragma unroll
;         for (int ai = 0; ai < 2; ++ai)
; #pragma unroll
;             for (int m = 0; m < 4; ++m) { float r[8];
; #pragma unroll
;                 for (int n = 0; n < 2; ++n)
; #pragma unroll
;                     for (int e = 0; e < 4; ++e) { const float g = acc[ai][0][m][n][e], up = acc[ai][1][m][n][e]; r[4 * n + e] = g * __builtin_amdgcn_rcpf(1.0f + __builtin_amdgcn_exp2f(-g * LOG2E)) * up * (float)(1 << ASHIFT); }
;                 v2u w; w.x = pk4_fp8(r[0], r[1], r[2], r[3]); w.y = pk4_fp8(r[4], r[5], r[6], r[7]);
;                 *(v2u*)(O + (size_t)(row0 + ai * HALF + m * 16) * EH + col0) = w; }
;     }
.LBB0_1661:
	s_mov_b32 s98, 0xbfb8aa3b
	s_mov_b32 s100, 0x41800000
	s_nop 15
	s_nop 15
	v_lshl_add_u32 v4, s87, 8, v203
	s_lshl_b32 s6, s88, 7
	s_and_b32 s6, s6, 0x180
	v_ashrrev_i32_e32 v5, 31, v4
	v_add_u32_e32 v2, s6, v205
	v_lshlrev_b64 v[0:1], 9, v[4:5]
	v_ashrrev_i32_e32 v3, 31, v2
	v_lshl_add_u64 v[0:1], s[24:25], 0, v[0:1]
	v_lshl_add_u64 v[0:1], v[0:1], 0, v[2:3]
	v_pk_mul_f32 v[228:229], v[192:193], s[98:99] op_sel_hi:[1,0]
	v_pk_mul_f32 v[230:231], v[194:195], s[98:99] op_sel_hi:[1,0]
	v_pk_mul_f32 v[232:233], v[184:185], s[98:99] op_sel_hi:[1,0]
	v_pk_mul_f32 v[234:235], v[186:187], s[98:99] op_sel_hi:[1,0]
	v_pk_mul_f32 v[236:237], v[176:177], s[98:99] op_sel_hi:[1,0]
	v_pk_mul_f32 v[238:239], v[178:179], s[98:99] op_sel_hi:[1,0]
	v_pk_mul_f32 v[240:241], v[168:169], s[98:99] op_sel_hi:[1,0]
	v_pk_mul_f32 v[242:243], v[170:171], s[98:99] op_sel_hi:[1,0]
	v_exp_f32_e32 v228, v228
	v_exp_f32_e32 v229, v229
	v_exp_f32_e32 v230, v230
	v_exp_f32_e32 v231, v231
	v_exp_f32_e32 v232, v232
	v_exp_f32_e32 v233, v233
	v_exp_f32_e32 v234, v234
	v_exp_f32_e32 v235, v235
	v_exp_f32_e32 v236, v236
	v_exp_f32_e32 v237, v237
	v_exp_f32_e32 v238, v238
	v_exp_f32_e32 v239, v239
	v_exp_f32_e32 v240, v240
	v_exp_f32_e32 v241, v241
	v_exp_f32_e32 v242, v242
	v_exp_f32_e32 v243, v243
	v_pk_add_f32 v[228:229], v[228:229], 1.0 op_sel_hi:[1,0]
	v_pk_add_f32 v[230:231], v[230:231], 1.0 op_sel_hi:[1,0]
	v_pk_add_f32 v[232:233], v[232:233], 1.0 op_sel_hi:[1,0]
	v_pk_add_f32 v[234:235], v[234:235], 1.0 op_sel_hi:[1,0]
	v_pk_add_f32 v[236:237], v[236:237], 1.0 op_sel_hi:[1,0]
	v_pk_add_f32 v[238:239], v[238:239], 1.0 op_sel_hi:[1,0]
	v_pk_add_f32 v[240:241], v[240:241], 1.0 op_sel_hi:[1,0]
	v_pk_add_f32 v[242:243], v[242:243], 1.0 op_sel_hi:[1,0]
	v_rcp_f32_e32 v228, v228
	v_rcp_f32_e32 v229, v229
	v_rcp_f32_e32 v230, v230
	v_rcp_f32_e32 v231, v231
	v_rcp_f32_e32 v232, v232
	v_rcp_f32_e32 v233, v233
	v_rcp_f32_e32 v234, v234
	v_rcp_f32_e32 v235, v235
	v_rcp_f32_e32 v236, v236
	v_rcp_f32_e32 v237, v237
	v_rcp_f32_e32 v238, v238
	v_rcp_f32_e32 v239, v239
	v_rcp_f32_e32 v240, v240
	v_rcp_f32_e32 v241, v241
	v_rcp_f32_e32 v242, v242
	v_rcp_f32_e32 v243, v243
	v_pk_mul_f32 v[228:229], v[192:193], v[228:229]
	v_pk_mul_f32 v[230:231], v[194:195], v[230:231]
	v_pk_mul_f32 v[232:233], v[184:185], v[232:233]
	v_pk_mul_f32 v[234:235], v[186:187], v[234:235]
	v_pk_mul_f32 v[236:237], v[176:177], v[236:237]
	v_pk_mul_f32 v[238:239], v[178:179], v[238:239]
	v_pk_mul_f32 v[240:241], v[168:169], v[240:241]
	v_pk_mul_f32 v[242:243], v[170:171], v[242:243]
	v_pk_mul_f32 v[228:229], v[188:189], v[228:229]
	v_pk_mul_f32 v[230:231], v[190:191], v[230:231]
	v_pk_mul_f32 v[232:233], v[180:181], v[232:233]
	v_pk_mul_f32 v[234:235], v[182:183], v[234:235]
	v_pk_mul_f32 v[236:237], v[172:173], v[236:237]
	v_pk_mul_f32 v[238:239], v[174:175], v[238:239]
	v_pk_mul_f32 v[240:241], v[164:165], v[240:241]
	v_pk_mul_f32 v[242:243], v[166:167], v[242:243]
	v_pk_mul_f32 v[228:229], s[100:101], v[228:229] op_sel_hi:[0,1]
	v_pk_mul_f32 v[230:231], s[100:101], v[230:231] op_sel_hi:[0,1]
	v_pk_mul_f32 v[232:233], s[100:101], v[232:233] op_sel_hi:[0,1]
	v_pk_mul_f32 v[234:235], s[100:101], v[234:235] op_sel_hi:[0,1]
	v_pk_mul_f32 v[236:237], s[100:101], v[236:237] op_sel_hi:[0,1]
	v_pk_mul_f32 v[238:239], s[100:101], v[238:239] op_sel_hi:[0,1]
	v_pk_mul_f32 v[240:241], s[100:101], v[240:241] op_sel_hi:[0,1]
	v_pk_mul_f32 v[242:243], s[100:101], v[242:243] op_sel_hi:[0,1]
	v_cvt_pk_fp8_f32 v244, v228, v229
	v_cvt_pk_fp8_f32 v245, v232, v233
	v_cvt_pk_fp8_f32 v246, v236, v237
	v_cvt_pk_fp8_f32 v247, v240, v241
	v_cvt_pk_fp8_f32 v244, v230, v231 op_sel:[0,0,1]
	v_cvt_pk_fp8_f32 v245, v234, v235 op_sel:[0,0,1]
	v_cvt_pk_fp8_f32 v246, v238, v239 op_sel:[0,0,1]
	v_cvt_pk_fp8_f32 v247, v242, v243 op_sel:[0,0,1]
	s_nop 0
	global_store_dwordx2 v[0:1], v[244:245], off
	v_or_b32_e32 v8, 16, v4
	v_ashrrev_i32_e32 v9, 31, v8
	v_lshlrev_b64 v[8:9], 9, v[8:9]
	v_lshl_add_u64 v[8:9], s[24:25], 0, v[8:9]
	v_lshl_add_u64 v[8:9], v[8:9], 0, v[2:3]
	global_store_dwordx2 v[8:9], v[246:247], off
	v_or_b32_e32 v8, 32, v4
	v_ashrrev_i32_e32 v9, 31, v8
	v_lshlrev_b64 v[8:9], 9, v[8:9]
	v_lshl_add_u64 v[8:9], s[24:25], 0, v[8:9]
	v_lshl_add_u64 v[8:9], v[8:9], 0, v[2:3]
	v_pk_mul_f32 v[228:229], v[160:161], s[98:99] op_sel_hi:[1,0]
	v_pk_mul_f32 v[230:231], v[162:163], s[98:99] op_sel_hi:[1,0]
	v_pk_mul_f32 v[232:233], v[152:153], s[98:99] op_sel_hi:[1,0]
	v_pk_mul_f32 v[234:235], v[154:155], s[98:99] op_sel_hi:[1,0]
	v_pk_mul_f32 v[236:237], v[144:145], s[98:99] op_sel_hi:[1,0]
	v_pk_mul_f32 v[238:239], v[146:147], s[98:99] op_sel_hi:[1,0]
	v_pk_mul_f32 v[240:241], v[136:137], s[98:99] op_sel_hi:[1,0]
	v_pk_mul_f32 v[242:243], v[138:139], s[98:99] op_sel_hi:[1,0]
	v_exp_f32_e32 v228, v228
	v_exp_f32_e32 v229, v229
	v_exp_f32_e32 v230, v230
	v_exp_f32_e32 v231, v231
	v_exp_f32_e32 v232, v232
	v_exp_f32_e32 v233, v233
	v_exp_f32_e32 v234, v234
	v_exp_f32_e32 v235, v235
	v_exp_f32_e32 v236, v236
	v_exp_f32_e32 v237, v237
	v_exp_f32_e32 v238, v238
	v_exp_f32_e32 v239, v239
	v_exp_f32_e32 v240, v240
	v_exp_f32_e32 v241, v241
	v_exp_f32_e32 v242, v242
	v_exp_f32_e32 v243, v243
	v_pk_add_f32 v[228:229], v[228:229], 1.0 op_sel_hi:[1,0]
	v_pk_add_f32 v[230:231], v[230:231], 1.0 op_sel_hi:[1,0]
	v_pk_add_f32 v[232:233], v[232:233], 1.0 op_sel_hi:[1,0]
	v_pk_add_f32 v[234:235], v[234:235], 1.0 op_sel_hi:[1,0]
	v_pk_add_f32 v[236:237], v[236:237], 1.0 op_sel_hi:[1,0]
	v_pk_add_f32 v[238:239], v[238:239], 1.0 op_sel_hi:[1,0]
	v_pk_add_f32 v[240:241], v[240:241], 1.0 op_sel_hi:[1,0]
	v_pk_add_f32 v[242:243], v[242:243], 1.0 op_sel_hi:[1,0]
; __device__ __forceinline__ unsigned pk4_fp8(float a, float b, float c, float d) { int r = __builtin_amdgcn_cvt_pk_fp8_f32(a, b, 0, false); r = __builtin_amdgcn_cvt_pk_fp8_f32(c, d, r, true); return (unsigned)r; }
;     __device__ __forceinline__ void operator()(const f32x4 (&acc)[2][2][4][2], const Unit& u, int wr, int wc, int fr, int fq) const {
;         const int row0 = u.pm * BM + wr * 64 + fr, col0 = (u.pn & 3) * 128 + wc * 32 + 8 * fq;
; #pragma unroll
;         for (int ai = 0; ai < 2; ++ai)
; #pragma unroll
;             for (int m = 0; m < 4; ++m) { float r[8];
; #pragma unroll
;                 for (int n = 0; n < 2; ++n)
; #pragma unroll
;                     for (int e = 0; e < 4; ++e) { const float g = acc[ai][0][m][n][e], up = acc[ai][1][m][n][e]; r[4 * n + e] = g * __builtin_amdgcn_rcpf(1.0f + __builtin_amdgcn_exp2f(-g * LOG2E)) * up * (float)(1 << ASHIFT); }
;                 v2u w; w.x = pk4_fp8(r[0], r[1], r[2], r[3]); w.y = pk4_fp8(r[4], r[5], r[6], r[7]);
;                 *(v2u*)(O + (size_t)(row0 + ai * HALF + m * 16) * EH + col0) = w; }
;     }
	v_rcp_f32_e32 v228, v228
	v_rcp_f32_e32 v229, v229
	v_rcp_f32_e32 v230, v230
	v_rcp_f32_e32 v231, v231
	v_rcp_f32_e32 v232, v232
	v_rcp_f32_e32 v233, v233
	v_rcp_f32_e32 v234, v234
	v_rcp_f32_e32 v235, v235
	v_rcp_f32_e32 v236, v236
	v_rcp_f32_e32 v237, v237
	v_rcp_f32_e32 v238, v238
	v_rcp_f32_e32 v239, v239
	v_rcp_f32_e32 v240, v240
	v_rcp_f32_e32 v241, v241
	v_rcp_f32_e32 v242, v242
	v_rcp_f32_e32 v243, v243
	v_pk_mul_f32 v[228:229], v[160:161], v[228:229]
	v_pk_mul_f32 v[230:231], v[162:163], v[230:231]
	v_pk_mul_f32 v[232:233], v[152:153], v[232:233]
	v_pk_mul_f32 v[234:235], v[154:155], v[234:235]
	v_pk_mul_f32 v[236:237], v[144:145], v[236:237]
	v_pk_mul_f32 v[238:239], v[146:147], v[238:239]
	v_pk_mul_f32 v[240:241], v[136:137], v[240:241]
	v_pk_mul_f32 v[242:243], v[138:139], v[242:243]
	v_pk_mul_f32 v[228:229], v[156:157], v[228:229]
	v_pk_mul_f32 v[230:231], v[158:159], v[230:231]
	v_pk_mul_f32 v[232:233], v[148:149], v[232:233]
	v_pk_mul_f32 v[234:235], v[150:151], v[234:235]
	v_pk_mul_f32 v[236:237], v[140:141], v[236:237]
	v_pk_mul_f32 v[238:239], v[142:143], v[238:239]
	v_pk_mul_f32 v[240:241], v[132:133], v[240:241]
	v_pk_mul_f32 v[242:243], v[134:135], v[242:243]
	v_pk_mul_f32 v[228:229], s[100:101], v[228:229] op_sel_hi:[0,1]
	v_pk_mul_f32 v[230:231], s[100:101], v[230:231] op_sel_hi:[0,1]
	v_pk_mul_f32 v[232:233], s[100:101], v[232:233] op_sel_hi:[0,1]
	v_pk_mul_f32 v[234:235], s[100:101], v[234:235] op_sel_hi:[0,1]
	v_pk_mul_f32 v[236:237], s[100:101], v[236:237] op_sel_hi:[0,1]
	v_pk_mul_f32 v[238:239], s[100:101], v[238:239] op_sel_hi:[0,1]
	v_pk_mul_f32 v[240:241], s[100:101], v[240:241] op_sel_hi:[0,1]
	v_pk_mul_f32 v[242:243], s[100:101], v[242:243] op_sel_hi:[0,1]
	v_cvt_pk_fp8_f32 v244, v228, v229
	v_cvt_pk_fp8_f32 v245, v232, v233
	v_cvt_pk_fp8_f32 v246, v236, v237
	v_cvt_pk_fp8_f32 v247, v240, v241
	v_cvt_pk_fp8_f32 v244, v230, v231 op_sel:[0,0,1]
	v_cvt_pk_fp8_f32 v245, v234, v235 op_sel:[0,0,1]
	v_cvt_pk_fp8_f32 v246, v238, v239 op_sel:[0,0,1]
	v_cvt_pk_fp8_f32 v247, v242, v243 op_sel:[0,0,1]
	s_nop 0
	global_store_dwordx2 v[8:9], v[244:245], off
	v_or_b32_e32 v4, 48, v4
	v_ashrrev_i32_e32 v5, 31, v4
	v_lshlrev_b64 v[4:5], 9, v[4:5]
	v_lshl_add_u64 v[4:5], s[24:25], 0, v[4:5]
	v_lshl_add_u64 v[2:3], v[4:5], 0, v[2:3]
	global_store_dwordx2 v[2:3], v[246:247], off
	v_add_co_u32_e32 v4, vcc, s50, v0
	s_nop 0
	v_addc_co_u32_e32 v5, vcc, 0, v1, vcc
	v_pk_mul_f32 v[228:229], v[128:129], s[98:99] op_sel_hi:[1,0]
	v_pk_mul_f32 v[230:231], v[130:131], s[98:99] op_sel_hi:[1,0]
	v_pk_mul_f32 v[232:233], v[120:121], s[98:99] op_sel_hi:[1,0]
	v_pk_mul_f32 v[234:235], v[122:123], s[98:99] op_sel_hi:[1,0]
	v_pk_mul_f32 v[236:237], v[112:113], s[98:99] op_sel_hi:[1,0]
	v_pk_mul_f32 v[238:239], v[114:115], s[98:99] op_sel_hi:[1,0]
	v_pk_mul_f32 v[240:241], v[104:105], s[98:99] op_sel_hi:[1,0]
	v_pk_mul_f32 v[242:243], v[106:107], s[98:99] op_sel_hi:[1,0]
	v_exp_f32_e32 v228, v228
	v_exp_f32_e32 v229, v229
	v_exp_f32_e32 v230, v230
	v_exp_f32_e32 v231, v231
	v_exp_f32_e32 v232, v232
	v_exp_f32_e32 v233, v233
	v_exp_f32_e32 v234, v234
	v_exp_f32_e32 v235, v235
	v_exp_f32_e32 v236, v236
	v_exp_f32_e32 v237, v237
	v_exp_f32_e32 v238, v238
	v_exp_f32_e32 v239, v239
	v_exp_f32_e32 v240, v240
	v_exp_f32_e32 v241, v241
	v_exp_f32_e32 v242, v242
	v_exp_f32_e32 v243, v243
	v_pk_add_f32 v[228:229], v[228:229], 1.0 op_sel_hi:[1,0]
	v_pk_add_f32 v[230:231], v[230:231], 1.0 op_sel_hi:[1,0]
	v_pk_add_f32 v[232:233], v[232:233], 1.0 op_sel_hi:[1,0]
	v_pk_add_f32 v[234:235], v[234:235], 1.0 op_sel_hi:[1,0]
	v_pk_add_f32 v[236:237], v[236:237], 1.0 op_sel_hi:[1,0]
	v_pk_add_f32 v[238:239], v[238:239], 1.0 op_sel_hi:[1,0]
	v_pk_add_f32 v[240:241], v[240:241], 1.0 op_sel_hi:[1,0]
	v_pk_add_f32 v[242:243], v[242:243], 1.0 op_sel_hi:[1,0]
	v_rcp_f32_e32 v228, v228
	v_rcp_f32_e32 v229, v229
	v_rcp_f32_e32 v230, v230
	v_rcp_f32_e32 v231, v231
	v_rcp_f32_e32 v232, v232
	v_rcp_f32_e32 v233, v233
	v_rcp_f32_e32 v234, v234
	v_rcp_f32_e32 v235, v235
	v_rcp_f32_e32 v236, v236
	v_rcp_f32_e32 v237, v237
	v_rcp_f32_e32 v238, v238
	v_rcp_f32_e32 v239, v239
	v_rcp_f32_e32 v240, v240
	v_rcp_f32_e32 v241, v241
	v_rcp_f32_e32 v242, v242
	v_rcp_f32_e32 v243, v243
	v_pk_mul_f32 v[228:229], v[128:129], v[228:229]
	v_pk_mul_f32 v[230:231], v[130:131], v[230:231]
	v_pk_mul_f32 v[232:233], v[120:121], v[232:233]
	v_pk_mul_f32 v[234:235], v[122:123], v[234:235]
	v_pk_mul_f32 v[236:237], v[112:113], v[236:237]
	v_pk_mul_f32 v[238:239], v[114:115], v[238:239]
	v_pk_mul_f32 v[240:241], v[104:105], v[240:241]
	v_pk_mul_f32 v[242:243], v[106:107], v[242:243]
	v_pk_mul_f32 v[228:229], v[124:125], v[228:229]
	v_pk_mul_f32 v[230:231], v[126:127], v[230:231]
	v_pk_mul_f32 v[232:233], v[116:117], v[232:233]
	v_pk_mul_f32 v[234:235], v[118:119], v[234:235]
	v_pk_mul_f32 v[236:237], v[108:109], v[236:237]
	v_pk_mul_f32 v[238:239], v[110:111], v[238:239]
	v_pk_mul_f32 v[240:241], v[100:101], v[240:241]
; __device__ __forceinline__ unsigned pk4_fp8(float a, float b, float c, float d) { int r = __builtin_amdgcn_cvt_pk_fp8_f32(a, b, 0, false); r = __builtin_amdgcn_cvt_pk_fp8_f32(c, d, r, true); return (unsigned)r; }
;     __device__ __forceinline__ void operator()(const f32x4 (&acc)[2][2][4][2], const Unit& u, int wr, int wc, int fr, int fq) const {
;         const int row0 = u.pm * BM + wr * 64 + fr, col0 = (u.pn & 3) * 128 + wc * 32 + 8 * fq;
; #pragma unroll
;         for (int ai = 0; ai < 2; ++ai)
; #pragma unroll
;             for (int m = 0; m < 4; ++m) { float r[8];
; #pragma unroll
;                 for (int n = 0; n < 2; ++n)
; #pragma unroll
;                     for (int e = 0; e < 4; ++e) { const float g = acc[ai][0][m][n][e], up = acc[ai][1][m][n][e]; r[4 * n + e] = g * __builtin_amdgcn_rcpf(1.0f + __builtin_amdgcn_exp2f(-g * LOG2E)) * up * (float)(1 << ASHIFT); }
;                 v2u w; w.x = pk4_fp8(r[0], r[1], r[2], r[3]); w.y = pk4_fp8(r[4], r[5], r[6], r[7]);
;                 *(v2u*)(O + (size_t)(row0 + ai * HALF + m * 16) * EH + col0) = w; }
;     }
	v_pk_mul_f32 v[242:243], v[102:103], v[242:243]
	v_pk_mul_f32 v[228:229], s[100:101], v[228:229] op_sel_hi:[0,1]
	v_pk_mul_f32 v[230:231], s[100:101], v[230:231] op_sel_hi:[0,1]
	v_pk_mul_f32 v[232:233], s[100:101], v[232:233] op_sel_hi:[0,1]
	v_pk_mul_f32 v[234:235], s[100:101], v[234:235] op_sel_hi:[0,1]
	v_pk_mul_f32 v[236:237], s[100:101], v[236:237] op_sel_hi:[0,1]
	v_pk_mul_f32 v[238:239], s[100:101], v[238:239] op_sel_hi:[0,1]
	v_pk_mul_f32 v[240:241], s[100:101], v[240:241] op_sel_hi:[0,1]
	v_pk_mul_f32 v[242:243], s[100:101], v[242:243] op_sel_hi:[0,1]
	v_cvt_pk_fp8_f32 v244, v228, v229
	v_cvt_pk_fp8_f32 v245, v232, v233
	v_cvt_pk_fp8_f32 v246, v236, v237
	v_cvt_pk_fp8_f32 v247, v240, v241
	v_cvt_pk_fp8_f32 v244, v230, v231 op_sel:[0,0,1]
	v_cvt_pk_fp8_f32 v245, v234, v235 op_sel:[0,0,1]
	v_cvt_pk_fp8_f32 v246, v238, v239 op_sel:[0,0,1]
	v_cvt_pk_fp8_f32 v247, v242, v243 op_sel:[0,0,1]
	s_nop 0
	global_store_dwordx2 v[4:5], v[244:245], off
	v_add_co_u32_e32 v4, vcc, s52, v0
	s_nop 0
	v_addc_co_u32_e32 v5, vcc, 0, v1, vcc
	global_store_dwordx2 v[4:5], v[246:247], off
	v_add_co_u32_e32 v4, vcc, s54, v0
	s_nop 0
	v_addc_co_u32_e32 v5, vcc, 0, v1, vcc
	v_pk_mul_f32 v[228:229], v[96:97], s[98:99] op_sel_hi:[1,0]
	v_pk_mul_f32 v[230:231], v[98:99], s[98:99] op_sel_hi:[1,0]
	v_pk_mul_f32 v[232:233], v[88:89], s[98:99] op_sel_hi:[1,0]
	v_pk_mul_f32 v[234:235], v[90:91], s[98:99] op_sel_hi:[1,0]
	v_pk_mul_f32 v[236:237], v[80:81], s[98:99] op_sel_hi:[1,0]
	v_pk_mul_f32 v[238:239], v[82:83], s[98:99] op_sel_hi:[1,0]
	v_pk_mul_f32 v[240:241], v[72:73], s[98:99] op_sel_hi:[1,0]
	v_pk_mul_f32 v[242:243], v[74:75], s[98:99] op_sel_hi:[1,0]
	v_exp_f32_e32 v228, v228
	v_exp_f32_e32 v229, v229
	v_exp_f32_e32 v230, v230
	v_exp_f32_e32 v231, v231
	v_exp_f32_e32 v232, v232
	v_exp_f32_e32 v233, v233
	v_exp_f32_e32 v234, v234
	v_exp_f32_e32 v235, v235
	v_exp_f32_e32 v236, v236
	v_exp_f32_e32 v237, v237
	v_exp_f32_e32 v238, v238
	v_exp_f32_e32 v239, v239
	v_exp_f32_e32 v240, v240
	v_exp_f32_e32 v241, v241
	v_exp_f32_e32 v242, v242
	v_exp_f32_e32 v243, v243
	v_pk_add_f32 v[228:229], v[228:229], 1.0 op_sel_hi:[1,0]
	v_pk_add_f32 v[230:231], v[230:231], 1.0 op_sel_hi:[1,0]
	v_pk_add_f32 v[232:233], v[232:233], 1.0 op_sel_hi:[1,0]
	v_pk_add_f32 v[234:235], v[234:235], 1.0 op_sel_hi:[1,0]
	v_pk_add_f32 v[236:237], v[236:237], 1.0 op_sel_hi:[1,0]
	v_pk_add_f32 v[238:239], v[238:239], 1.0 op_sel_hi:[1,0]
	v_pk_add_f32 v[240:241], v[240:241], 1.0 op_sel_hi:[1,0]
	v_pk_add_f32 v[242:243], v[242:243], 1.0 op_sel_hi:[1,0]
	v_rcp_f32_e32 v228, v228
	v_rcp_f32_e32 v229, v229
	v_rcp_f32_e32 v230, v230
	v_rcp_f32_e32 v231, v231
	v_rcp_f32_e32 v232, v232
	v_rcp_f32_e32 v233, v233
	v_rcp_f32_e32 v234, v234
	v_rcp_f32_e32 v235, v235
	v_rcp_f32_e32 v236, v236
	v_rcp_f32_e32 v237, v237
	v_rcp_f32_e32 v238, v238
	v_rcp_f32_e32 v239, v239
	v_rcp_f32_e32 v240, v240
	v_rcp_f32_e32 v241, v241
	v_rcp_f32_e32 v242, v242
	v_rcp_f32_e32 v243, v243
	v_pk_mul_f32 v[228:229], v[96:97], v[228:229]
	v_pk_mul_f32 v[230:231], v[98:99], v[230:231]
	v_pk_mul_f32 v[232:233], v[88:89], v[232:233]
	v_pk_mul_f32 v[234:235], v[90:91], v[234:235]
	v_pk_mul_f32 v[236:237], v[80:81], v[236:237]
	v_pk_mul_f32 v[238:239], v[82:83], v[238:239]
	v_pk_mul_f32 v[240:241], v[72:73], v[240:241]
	v_pk_mul_f32 v[242:243], v[74:75], v[242:243]
	v_pk_mul_f32 v[228:229], v[92:93], v[228:229]
	v_pk_mul_f32 v[230:231], v[94:95], v[230:231]
	v_pk_mul_f32 v[232:233], v[84:85], v[232:233]
	v_pk_mul_f32 v[234:235], v[86:87], v[234:235]
	v_pk_mul_f32 v[236:237], v[76:77], v[236:237]
	v_pk_mul_f32 v[238:239], v[78:79], v[238:239]
	v_pk_mul_f32 v[240:241], v[68:69], v[240:241]
	v_pk_mul_f32 v[242:243], v[70:71], v[242:243]
	v_pk_mul_f32 v[228:229], s[100:101], v[228:229] op_sel_hi:[0,1]
	v_pk_mul_f32 v[230:231], s[100:101], v[230:231] op_sel_hi:[0,1]
	v_pk_mul_f32 v[232:233], s[100:101], v[232:233] op_sel_hi:[0,1]
	v_pk_mul_f32 v[234:235], s[100:101], v[234:235] op_sel_hi:[0,1]
	v_pk_mul_f32 v[236:237], s[100:101], v[236:237] op_sel_hi:[0,1]
	v_pk_mul_f32 v[238:239], s[100:101], v[238:239] op_sel_hi:[0,1]
	v_pk_mul_f32 v[240:241], s[100:101], v[240:241] op_sel_hi:[0,1]
	v_pk_mul_f32 v[242:243], s[100:101], v[242:243] op_sel_hi:[0,1]
	v_cvt_pk_fp8_f32 v244, v228, v229
	v_cvt_pk_fp8_f32 v245, v232, v233
	v_cvt_pk_fp8_f32 v246, v236, v237
	v_cvt_pk_fp8_f32 v247, v240, v241
	v_cvt_pk_fp8_f32 v244, v230, v231 op_sel:[0,0,1]
	v_cvt_pk_fp8_f32 v245, v234, v235 op_sel:[0,0,1]
	v_cvt_pk_fp8_f32 v246, v238, v239 op_sel:[0,0,1]
	v_cvt_pk_fp8_f32 v247, v242, v243 op_sel:[0,0,1]
	s_nop 0
	global_store_dwordx2 v[4:5], v[244:245], off
	v_add_co_u32_e32 v0, vcc, 0x16000, v0
	s_nop 1
	v_addc_co_u32_e32 v1, vcc, 0, v1, vcc
	s_and_b64 vcc, exec, s[4:5]
	s_mov_b64 s[4:5], -1
	global_store_dwordx2 v[0:1], v[246:247], off
	s_cbranch_vccnz .LBB0_1625
	s_andn2_b64 vcc, exec, s[22:23]
	s_cbranch_vccnz .LBB0_1624
	s_barrier
	s_branch .LBB0_1624
